# v14 + workgroups without a router-GEMM tile (P11) convert the last chunk of every workgroup
# speedup vs baseline: 1.0112x; 1.0026x over previous
.LBB0_2419:
	s_lshl_b32 s2, s2, 13
	s_add_i32 s76, s2, 0
	s_add_i32 s76, s76, 0x10000
	s_andn2_b64 vcc, exec, s[8:9]
	v_lshlrev_b32_e32 v134, 2, v162
	s_cbranch_vccnz .LBB0_2468
	v_or_b32_e32 v6, 32, v168
	v_cmp_gt_i32_e64 s[40:41], v6, v2
	v_cmp_lt_i32_e64 s[42:43], v6, v2
	v_or_b32_e32 v6, 34, v168
	v_cmp_gt_i32_e64 s[44:45], v6, v2
	v_or_b32_e32 v6, 35, v168
	v_cmp_gt_i32_e64 s[46:47], v6, v2
	v_or_b32_e32 v6, 40, v168
	v_cmp_gt_i32_e64 s[48:49], v6, v2
	v_or_b32_e32 v6, 41, v168
	v_cmp_gt_i32_e64 s[50:51], v6, v2
	v_or_b32_e32 v6, 42, v168
	v_cmp_gt_i32_e64 s[52:53], v6, v2
	v_or_b32_e32 v6, 43, v168
	v_cmp_gt_i32_e64 s[54:55], v6, v2
	v_or_b32_e32 v6, 48, v168
	v_cmp_gt_i32_e64 s[56:57], v6, v2
	v_or_b32_e32 v6, 49, v168
	v_cmp_gt_i32_e64 s[58:59], v6, v2
	v_or_b32_e32 v6, 50, v168
	v_cmp_gt_i32_e64 s[60:61], v6, v2
	v_or_b32_e32 v6, 51, v168
	v_cmp_gt_i32_e64 s[62:63], v6, v2
	v_or_b32_e32 v6, 56, v168
	v_cmp_gt_i32_e64 s[64:65], v6, v2
	v_or_b32_e32 v6, 57, v168
	v_cmp_gt_i32_e64 s[66:67], v6, v2
	v_or_b32_e32 v6, 58, v168
	v_cmp_gt_i32_e64 s[68:69], v6, v2
	v_or_b32_e32 v6, 59, v168
	v_cmp_gt_i32_e64 s[6:7], v168, v2
	v_cmp_lt_i32_e64 s[8:9], v168, v2
	v_cmp_gt_i32_e64 s[10:11], v135, v2
	v_cmp_gt_i32_e64 s[12:13], v169, v2
	v_cmp_gt_i32_e64 s[14:15], v170, v2
	v_cmp_gt_i32_e64 s[16:17], v171, v2
	v_cmp_gt_i32_e64 s[18:19], v172, v2
	v_cmp_gt_i32_e64 s[20:21], v173, v2
	v_cmp_gt_i32_e64 s[22:23], v174, v2
	v_cmp_gt_i32_e64 s[24:25], v175, v2
	v_cmp_gt_i32_e64 s[26:27], v176, v2
	v_cmp_gt_i32_e64 s[28:29], v177, v2
	v_cmp_gt_i32_e64 s[30:31], v178, v2
	v_cmp_gt_i32_e64 s[34:35], v179, v2
	v_cmp_gt_i32_e64 s[36:37], v180, v2
	v_cmp_gt_i32_e64 s[38:39], v181, v2
	v_cmp_gt_i32_e64 s[70:71], v6, v2
	s_min_u32 s2, s92, 8
	v_lshlrev_b32_e32 v2, 4, v4
	s_add_i32 s2, s92, s2
	v_and_b32_e32 v2, 0xc0, v2
	s_lshl_b32 s87, s2, 13
	v_lshl_or_b32 v2, v160, 8, v2
	v_readlane_b32 s2, v247, 4
	v_lshlrev_b32_e32 v5, 1, v4
	v_mov_b32_e32 v140, 0
	v_add_u32_e32 v185, s2, v2
	v_readlane_b32 s2, v247, 5
	s_movk_i32 s96, 0xc00
	s_add_i32 s91, s91, s92
	v_add_u32_e32 v187, s2, v2
	v_readlane_b32 s2, v247, 6
	s_add_i32 s93, s93, s3
	v_mov_b32_e32 v139, v131
	v_add_u32_e32 v188, s2, v2
	v_readlane_b32 s2, v247, 7
	s_mov_b32 s94, 2
	v_add_u32_e32 v183, s75, v134
	v_add_u32_e32 v189, s2, v2
	v_readlane_b32 s2, v247, 8
	v_add3_u32 v184, s76, v166, v134
	s_lshl_b32 s95, s92, 13
	v_add_u32_e32 v190, s2, v2
	v_readlane_b32 s2, v247, 9
	s_addk_i32 s87, 0x4000
	v_and_or_b32 v186, v5, 32, v3
	v_add_u32_e32 v191, s2, v2
	v_readlane_b32 s2, v247, 10
	s_add_i32 s86, s75, 0xc000
	s_mov_b32 s3, 0
	v_add_u32_e32 v192, s2, v2
	v_readlane_b32 s2, v247, 11
	v_mov_b32_e32 v202, 0
	v_mov_b32_e32 v3, v140
	v_add_u32_e32 v193, s2, v2
	v_readlane_b32 s2, v247, 12
	v_mov_b32_e32 v4, v140
	v_mov_b32_e32 v5, v140
	v_add_u32_e32 v194, s2, v2
	v_readlane_b32 s2, v247, 13
	v_mov_b32_e32 v6, v140
	v_mov_b32_e32 v7, v140
	v_add_u32_e32 v195, s2, v2
	v_readlane_b32 s2, v247, 14
	v_mov_b32_e32 v8, v140
	v_mov_b32_e32 v9, v140
	v_add_u32_e32 v196, s2, v2
	v_readlane_b32 s2, v247, 15
	v_mov_b32_e32 v10, v140
	v_mov_b32_e32 v11, v140
	v_add_u32_e32 v197, s2, v2
	v_readlane_b32 s2, v247, 16
	v_mov_b32_e32 v12, v140
	v_mov_b32_e32 v13, v140
	v_add_u32_e32 v198, s2, v2
	v_readlane_b32 s2, v247, 17
	v_mov_b32_e32 v14, v140
	v_mov_b32_e32 v15, v140
	v_add_u32_e32 v199, s2, v2
	v_readlane_b32 s2, v247, 21
	v_mov_b32_e32 v16, v140
	v_mov_b32_e32 v17, v140
	v_add_u32_e32 v200, s2, v2
	s_add_i32 s2, 0, 0x8000
	v_add_u32_e32 v201, s2, v2
	s_mov_b32 s2, 0
	v_mov_b32_e32 v2, 0
	v_mov_b32_e32 v18, 0
	v_mov_b32_e32 v19, v140
	v_mov_b32_e32 v20, v140
	v_mov_b32_e32 v21, v140
	v_mov_b32_e32 v22, v140
	v_mov_b32_e32 v23, v140
	v_add_u32_e32 v226, v201, v186
	s_nop 0
	s_nop 0
	s_nop 0
	s_nop 0
	s_nop 0
	s_nop 0
	s_nop 0
	v_mov_b32_e32 v24, v140
	v_mov_b32_e32 v25, v140
	v_mov_b32_e32 v26, v140
	v_mov_b32_e32 v27, v140
	v_mov_b32_e32 v28, v140
	v_mov_b32_e32 v29, v140
	v_mov_b32_e32 v30, v140
	v_mov_b32_e32 v31, v140
	v_mov_b32_e32 v32, v140
	v_mov_b32_e32 v33, v140
	v_mov_b64_e32 v[50:51], v[98:99]
	v_mov_b64_e32 v[52:53], v[100:101]
	v_mov_b64_e32 v[54:55], v[102:103]
	v_mov_b64_e32 v[56:57], v[104:105]
	v_mov_b64_e32 v[58:59], v[106:107]
	v_mov_b64_e32 v[60:61], v[108:109]
	v_mov_b64_e32 v[62:63], v[110:111]
	v_mov_b64_e32 v[64:65], v[112:113]
	s_mov_b32 s32, 0
	v_readlane_b32 s72, v249, 50
	s_cmp_gt_i32 s72, 6
	s_cbranch_scc1 .LBB0_2422
	s_mul_i32 s72, s72, 48
	v_readlane_b32 s73, v248, 47
	s_add_i32 s72, s73, s72
	v_readlane_b32 s78, v248, 48
	s_add_i32 s73, s72, 48
	s_min_i32 s78, s78, s73
	s_min_i32 s78, s78, 0x1be90
	v_readlane_b32 s84, v249, 16
	s_add_i32 s73, s72, s84
	s_cmp_ge_i32 s73, s78
	s_cbranch_scc1 .LBB0_2422
	v_writelane_b32 v244, s78, 3
	s_lshl_b32 s84, s84, 11
	s_add_i32 s84, s84, 0x24000
	v_and_b32_e32 v82, 63, v0
	v_and_b32_e32 v83, 31, v82
	v_lshrrev_b32_e32 v84, 5, v82
	v_lshlrev_b32_e32 v84, 10, v84
	v_lshl_add_u32 v83, v83, 2, v84
	v_add_u32_e32 v245, s84, v83
	s_mov_b32 s85, 2
	s_mov_b32 s32, 0x30
	s_branch .Lbgn_dec

.LBB0_2471:
	s_or_b64 exec, exec, s[6:7]
	s_waitcnt lgkmcnt(0)
	v_lshl_add_u32 v51, v160, 4, s75
	v_add3_u32 v50, s76, v166, v134
	ds_read_b32 v54, v51 offset:57472
	ds_read2_b32 v[52:53], v50 offset1:32
	s_lshl_b32 s2, s2, 1
	v_readlane_b32 s3, v249, 61
	s_add_u32 s2, s3, s2
	v_readlane_b32 s3, v249, 36
	s_waitcnt lgkmcnt(0)
	v_fma_f32 v2, v2, v54, v52
	v_fmac_f32_e32 v53, v18, v54
	ds_write2_b32 v50, v2, v53 offset1:32
	ds_read_b32 v2, v51 offset:57476
	ds_read2_b32 v[52:53], v50 offset0:64 offset1:96
	s_addc_u32 s3, s3, 0
	s_waitcnt lgkmcnt(0)
	v_fma_f32 v3, v3, v2, v52
	v_fmac_f32_e32 v53, v19, v2
	ds_write2_b32 v50, v3, v53 offset0:64 offset1:96
	ds_read_b32 v18, v51 offset:57480
	ds_read2_b32 v[2:3], v50 offset0:128 offset1:160
	v_add_u32_e32 v19, 0x1000, v50
	s_waitcnt lgkmcnt(0)
	v_fma_f32 v2, v4, v18, v2
	v_fmac_f32_e32 v3, v20, v18
	ds_write2_b32 v50, v2, v3 offset0:128 offset1:160
	ds_read_b32 v4, v51 offset:57484
	ds_read2_b32 v[2:3], v50 offset0:192 offset1:224
	v_add_u32_e32 v18, 0x800, v50
	v_add_u32_e32 v20, 0x1800, v50
	s_waitcnt lgkmcnt(0)
	v_fma_f32 v2, v5, v4, v2
	v_fmac_f32_e32 v3, v21, v4
	ds_write2_b32 v50, v2, v3 offset0:192 offset1:224
	ds_read_b32 v4, v51 offset:57504
	ds_read2_b32 v[2:3], v18 offset1:32
	s_waitcnt lgkmcnt(0)
	v_fma_f32 v2, v6, v4, v2
	v_fmac_f32_e32 v3, v22, v4
	ds_write2_b32 v18, v2, v3 offset1:32
	ds_read_b32 v4, v51 offset:57508
	ds_read2_b32 v[2:3], v18 offset0:64 offset1:96
	s_waitcnt lgkmcnt(0)
	v_fma_f32 v2, v7, v4, v2
	v_fmac_f32_e32 v3, v23, v4
	ds_write2_b32 v18, v2, v3 offset0:64 offset1:96
	ds_read_b32 v4, v51 offset:57512
	ds_read2_b32 v[2:3], v18 offset0:128 offset1:160
	s_waitcnt lgkmcnt(0)
	v_fma_f32 v2, v8, v4, v2
	v_fmac_f32_e32 v3, v24, v4
	ds_write2_b32 v18, v2, v3 offset0:128 offset1:160
	ds_read_b32 v4, v51 offset:57516
	ds_read2_b32 v[2:3], v18 offset0:192 offset1:224
	s_waitcnt lgkmcnt(0)
	v_fma_f32 v2, v9, v4, v2
	v_fmac_f32_e32 v3, v25, v4
	ds_write2_b32 v18, v2, v3 offset0:192 offset1:224
	ds_read_b32 v4, v51 offset:57536
	ds_read2_b32 v[2:3], v19 offset1:32
	s_waitcnt lgkmcnt(0)
	v_fma_f32 v2, v10, v4, v2
	v_fmac_f32_e32 v3, v26, v4
	ds_write2_b32 v19, v2, v3 offset1:32
	ds_read_b32 v4, v51 offset:57540
	ds_read2_b32 v[2:3], v19 offset0:64 offset1:96
	s_waitcnt lgkmcnt(0)
	v_fma_f32 v2, v11, v4, v2
	v_fmac_f32_e32 v3, v27, v4
	ds_write2_b32 v19, v2, v3 offset0:64 offset1:96
	ds_read_b32 v4, v51 offset:57544
	ds_read2_b32 v[2:3], v19 offset0:128 offset1:160
	s_waitcnt lgkmcnt(0)
	v_fma_f32 v2, v12, v4, v2
	v_fmac_f32_e32 v3, v28, v4
	ds_write2_b32 v19, v2, v3 offset0:128 offset1:160
	ds_read_b32 v4, v51 offset:57548
	ds_read2_b32 v[2:3], v19 offset0:192 offset1:224
	s_waitcnt lgkmcnt(0)
	v_fma_f32 v2, v13, v4, v2
	v_fmac_f32_e32 v3, v29, v4
	ds_write2_b32 v19, v2, v3 offset0:192 offset1:224
	ds_read_b32 v4, v51 offset:57568
	ds_read2_b32 v[2:3], v20 offset1:32
	s_waitcnt lgkmcnt(0)
	v_fma_f32 v2, v14, v4, v2
	v_fmac_f32_e32 v3, v30, v4
	ds_write2_b32 v20, v2, v3 offset1:32
	ds_read_b32 v4, v51 offset:57572
	ds_read2_b32 v[2:3], v20 offset0:64 offset1:96
	s_waitcnt lgkmcnt(0)
	v_fma_f32 v2, v15, v4, v2
	v_fmac_f32_e32 v3, v31, v4
	ds_write2_b32 v20, v2, v3 offset0:64 offset1:96
	ds_read_b32 v4, v51 offset:57576
	ds_read2_b32 v[2:3], v20 offset0:128 offset1:160
	s_waitcnt lgkmcnt(0)
	v_fma_f32 v2, v16, v4, v2
	v_fmac_f32_e32 v3, v32, v4
	ds_write2_b32 v20, v2, v3 offset0:128 offset1:160
	ds_read_b32 v4, v51 offset:57580
	ds_read2_b32 v[2:3], v20 offset0:192 offset1:224
	s_waitcnt lgkmcnt(0)
	v_fma_f32 v2, v17, v4, v2
	v_fmac_f32_e32 v3, v33, v4
	ds_write2_b32 v20, v2, v3 offset0:192 offset1:224
	v_mov_b64_e32 v[2:3], v[66:67]
	s_waitcnt lgkmcnt(0)
	v_mov_b64_e32 v[4:5], v[68:69]
	v_mov_b64_e32 v[6:7], v[70:71]
	v_mov_b64_e32 v[8:9], v[72:73]
	v_mov_b64_e32 v[10:11], v[74:75]
	v_mov_b64_e32 v[12:13], v[76:77]
	v_mov_b64_e32 v[14:15], v[78:79]
	v_mov_b64_e32 v[16:17], v[80:81]
	ds_read2_b32 v[2:3], v50 offset1:32
	s_waitcnt vmcnt(31) lgkmcnt(0)
	v_add_f32_e32 v4, v96, v2
	s_waitcnt vmcnt(30)
	v_add_f32_e32 v5, v97, v3
	ds_read2_b32 v[2:3], v50 offset0:64 offset1:96
	s_waitcnt vmcnt(29) lgkmcnt(0)
	v_add_f32_e32 v6, v94, v2
	s_waitcnt vmcnt(28)
	v_add_f32_e32 v7, v95, v3
	ds_read2_b32 v[2:3], v50 offset0:128 offset1:160
	s_waitcnt vmcnt(27) lgkmcnt(0)
	v_add_f32_e32 v8, v92, v2
	s_waitcnt vmcnt(26)
	v_add_f32_e32 v9, v93, v3
	ds_read2_b32 v[2:3], v50 offset0:192 offset1:224
	s_waitcnt vmcnt(25) lgkmcnt(0)
	v_add_f32_e32 v10, v90, v2
	s_waitcnt vmcnt(24)
	v_add_f32_e32 v11, v91, v3
	ds_read2_b32 v[2:3], v18 offset1:32
	s_waitcnt vmcnt(23) lgkmcnt(0)
	v_add_f32_e32 v12, v86, v2
	s_waitcnt vmcnt(22)
	v_add_f32_e32 v13, v87, v3
	ds_read2_b32 v[2:3], v18 offset0:64 offset1:96
	s_waitcnt vmcnt(21) lgkmcnt(0)
	v_add_f32_e32 v14, v84, v2
	s_waitcnt vmcnt(20)
	v_add_f32_e32 v15, v85, v3
	ds_read2_b32 v[2:3], v18 offset0:128 offset1:160
	s_waitcnt vmcnt(19) lgkmcnt(0)
	v_add_f32_e32 v16, v82, v2
	s_waitcnt vmcnt(18)
	v_add_f32_e32 v17, v83, v3
	ds_read2_b32 v[2:3], v18 offset0:192 offset1:224
	s_waitcnt vmcnt(17) lgkmcnt(0)
	v_add_f32_e32 v18, v46, v2
	s_waitcnt vmcnt(16)
	v_add_f32_e32 v21, v47, v3
	ds_read2_b32 v[2:3], v19 offset1:32
	s_waitcnt vmcnt(15) lgkmcnt(0)
	v_add_f32_e32 v22, v58, v2
	s_waitcnt vmcnt(14)
	v_add_f32_e32 v23, v59, v3
	ds_read2_b32 v[2:3], v19 offset0:64 offset1:96
	s_waitcnt vmcnt(13) lgkmcnt(0)
	v_add_f32_e32 v24, v48, v2
	s_waitcnt vmcnt(12)
	v_add_f32_e32 v25, v49, v3
	ds_read2_b32 v[2:3], v19 offset0:128 offset1:160
	s_waitcnt vmcnt(11) lgkmcnt(0)
	v_add_f32_e32 v26, v44, v2
	s_waitcnt vmcnt(10)
	v_add_f32_e32 v27, v45, v3
	ds_read2_b32 v[2:3], v19 offset0:192 offset1:224
	s_waitcnt vmcnt(9) lgkmcnt(0)
	v_add_f32_e32 v19, v40, v2
	s_waitcnt vmcnt(8)
	v_add_f32_e32 v28, v41, v3
	ds_read2_b32 v[2:3], v20 offset1:32
	s_waitcnt vmcnt(7) lgkmcnt(0)
	v_add_f32_e32 v29, v42, v2
	s_waitcnt vmcnt(6)
	v_add_f32_e32 v30, v43, v3
	ds_read2_b32 v[2:3], v20 offset0:64 offset1:96
	s_waitcnt vmcnt(5) lgkmcnt(0)
	v_add_f32_e32 v31, v38, v2
	s_waitcnt vmcnt(4)
	v_add_f32_e32 v32, v39, v3
	ds_read2_b32 v[2:3], v20 offset0:128 offset1:160
	s_waitcnt vmcnt(3) lgkmcnt(0)
	v_add_f32_e32 v33, v36, v2
	s_waitcnt vmcnt(2)
	v_add_f32_e32 v36, v37, v3
	ds_read2_b32 v[2:3], v20 offset0:192 offset1:224
	v_lshlrev_b32_e32 v20, 9, v160
	s_waitcnt lgkmcnt(0)
	s_waitcnt vmcnt(1) lgkmcnt(0)
	v_add_f32_e32 v2, v34, v2
	v_lshlrev_b32_e32 v34, 1, v162
	v_add3_u32 v20, s76, v20, v34
	v_bfe_u32 v34, v4, 16, 1
	v_add3_u32 v4, v4, v34, s74
	ds_write_b16_d16_hi v20, v4
	v_bfe_u32 v4, v5, 16, 1
	v_add3_u32 v4, v5, v4, s74
	ds_write_b16_d16_hi v20, v4 offset:64
	v_bfe_u32 v4, v6, 16, 1
	v_add3_u32 v4, v6, v4, s74
	ds_write_b16_d16_hi v20, v4 offset:128
	v_bfe_u32 v4, v7, 16, 1
	v_add3_u32 v4, v7, v4, s74
	ds_write_b16_d16_hi v20, v4 offset:192
	v_bfe_u32 v4, v8, 16, 1
	v_add3_u32 v4, v8, v4, s74
	ds_write_b16_d16_hi v20, v4 offset:256
	v_bfe_u32 v4, v9, 16, 1
	v_add3_u32 v4, v9, v4, s74
	ds_write_b16_d16_hi v20, v4 offset:320
	v_bfe_u32 v4, v10, 16, 1
	v_add3_u32 v4, v10, v4, s74
	ds_write_b16_d16_hi v20, v4 offset:384
	v_bfe_u32 v4, v11, 16, 1
	v_add3_u32 v4, v11, v4, s74
	ds_write_b16_d16_hi v20, v4 offset:448
	v_bfe_u32 v4, v12, 16, 1
	v_add3_u32 v4, v12, v4, s74
	ds_write_b16_d16_hi v20, v4 offset:1024
	v_bfe_u32 v4, v13, 16, 1
	v_add3_u32 v4, v13, v4, s74
	ds_write_b16_d16_hi v20, v4 offset:1088
	v_bfe_u32 v4, v14, 16, 1
	v_add3_u32 v4, v14, v4, s74
	ds_write_b16_d16_hi v20, v4 offset:1152
	v_bfe_u32 v4, v15, 16, 1
	v_add3_u32 v4, v15, v4, s74
	ds_write_b16_d16_hi v20, v4 offset:1216
	v_bfe_u32 v4, v16, 16, 1
	v_add3_u32 v4, v16, v4, s74
	ds_write_b16_d16_hi v20, v4 offset:1280
	v_bfe_u32 v4, v17, 16, 1
	v_add3_u32 v4, v17, v4, s74
	ds_write_b16_d16_hi v20, v4 offset:1344
	v_bfe_u32 v4, v18, 16, 1
	v_add3_u32 v4, v18, v4, s74
	ds_write_b16_d16_hi v20, v4 offset:1408
	v_bfe_u32 v4, v21, 16, 1
	v_add3_u32 v4, v21, v4, s74
	ds_write_b16_d16_hi v20, v4 offset:1472
	v_bfe_u32 v4, v22, 16, 1
	v_add3_u32 v4, v22, v4, s74
	ds_write_b16_d16_hi v20, v4 offset:2048
	v_bfe_u32 v4, v23, 16, 1
	v_add3_u32 v4, v23, v4, s74
	ds_write_b16_d16_hi v20, v4 offset:2112
	v_bfe_u32 v4, v24, 16, 1
	v_add3_u32 v4, v24, v4, s74
	ds_write_b16_d16_hi v20, v4 offset:2176
	v_bfe_u32 v4, v25, 16, 1
	v_add3_u32 v4, v25, v4, s74
	ds_write_b16_d16_hi v20, v4 offset:2240
	v_bfe_u32 v4, v26, 16, 1
	v_add3_u32 v4, v26, v4, s74
	ds_write_b16_d16_hi v20, v4 offset:2304
	v_bfe_u32 v4, v27, 16, 1
	v_add3_u32 v4, v27, v4, s74
	ds_write_b16_d16_hi v20, v4 offset:2368
	v_bfe_u32 v4, v19, 16, 1
	v_add3_u32 v4, v19, v4, s74
	ds_write_b16_d16_hi v20, v4 offset:2432
	v_bfe_u32 v4, v28, 16, 1
	v_add3_u32 v4, v28, v4, s74
	ds_write_b16_d16_hi v20, v4 offset:2496
	v_bfe_u32 v4, v29, 16, 1
	v_add3_u32 v4, v29, v4, s74
	ds_write_b16_d16_hi v20, v4 offset:3072
	v_bfe_u32 v4, v30, 16, 1
	v_add3_u32 v4, v30, v4, s74
	ds_write_b16_d16_hi v20, v4 offset:3136
	v_bfe_u32 v4, v31, 16, 1
	v_add3_u32 v4, v31, v4, s74
	ds_write_b16_d16_hi v20, v4 offset:3200
	v_bfe_u32 v4, v32, 16, 1
	v_add3_u32 v4, v32, v4, s74
	ds_write_b16_d16_hi v20, v4 offset:3264
	v_bfe_u32 v4, v33, 16, 1
	v_add3_u32 v4, v33, v4, s74
	ds_write_b16_d16_hi v20, v4 offset:3328
	v_bfe_u32 v4, v36, 16, 1
	v_add3_u32 v4, v36, v4, s74
	ds_write_b16_d16_hi v20, v4 offset:3392
	v_bfe_u32 v4, v2, 16, 1
	s_waitcnt vmcnt(0)
	v_add_f32_e32 v3, v35, v3
	v_add3_u32 v2, v2, v4, s74
	ds_write_b16_d16_hi v20, v2 offset:3456
	v_bfe_u32 v2, v3, 16, 1
	v_add3_u32 v2, v3, v2, s74
	ds_write_b16_d16_hi v20, v2 offset:3520
	v_lshlrev_b32_e32 v2, 1, v158
	v_and_b32_e32 v130, 0x70, v2
	s_waitcnt lgkmcnt(0)
	v_lshrrev_b32_e32 v12, 3, v137
	v_add_u32_e32 v13, s76, v130
	v_lshl_add_u32 v2, v12, 7, v13
	ds_read_b128 v[2:5], v2
	v_or_b32_e32 v8, s0, v12
	v_mov_b32_e32 v9, s1
	v_lshl_add_u64 v[6:7], s[2:3], 0, v[130:131]
	v_lshlrev_b64 v[10:11], 12, v[8:9]
	v_lshl_add_u64 v[10:11], v[6:7], 0, v[10:11]
	v_or_b32_e32 v8, 8, v12
	s_waitcnt lgkmcnt(0)
	global_store_dwordx4 v[10:11], v[2:5], off
	s_nop 1
	v_lshl_add_u32 v2, v8, 7, v13
	ds_read_b128 v[2:5], v2
	v_or_b32_e32 v8, s0, v8
	v_lshlrev_b64 v[10:11], 12, v[8:9]
	v_lshl_add_u64 v[10:11], v[6:7], 0, v[10:11]
	v_or_b32_e32 v8, 16, v12
	s_waitcnt lgkmcnt(0)
	global_store_dwordx4 v[10:11], v[2:5], off
	s_nop 1
	v_lshl_add_u32 v2, v8, 7, v13
	ds_read_b128 v[2:5], v2
	v_or_b32_e32 v8, s0, v8
	v_lshlrev_b64 v[10:11], 12, v[8:9]
	v_lshl_add_u64 v[10:11], v[6:7], 0, v[10:11]
	v_or_b32_e32 v8, 24, v12
	s_waitcnt lgkmcnt(0)
	global_store_dwordx4 v[10:11], v[2:5], off
	s_nop 1
	v_lshl_add_u32 v2, v8, 7, v13
	ds_read_b128 v[2:5], v2
	v_or_b32_e32 v8, s0, v8
	v_lshlrev_b64 v[8:9], 12, v[8:9]
	v_lshl_add_u64 v[6:7], v[6:7], 0, v[8:9]
	s_waitcnt lgkmcnt(0)
	global_store_dwordx4 v[6:7], v[2:5], off
	s_waitcnt lgkmcnt(0)
	s_barrier
	s_setprio 0
	v_readlane_b32 s42, v249, 26
	v_readlane_b32 s50, v249, 30
	s_cmp_gt_i32 s60, 6
	v_readlane_b32 s43, v249, 27
	v_readlane_b32 s51, v249, 31
	s_cbranch_scc1 .LBB0_2336
	s_mul_i32 s0, s60, 48
	v_readlane_b32 s1, v248, 47
	s_add_i32 s6, s1, s0
	v_readlane_b32 s1, v248, 48
	s_add_i32 s0, s6, 48
	s_cmp_lg_u32 s60, 0
	v_mov_b32_e32 v2, s1
	v_min3_i32 v2, s0, v2, v165
	s_nop 0
	v_readfirstlane_b32 s26, v2
	s_nop 0
	s_nop 0
	s_nop 0
	s_nop 0
	s_nop 0
	s_nop 0
	s_nop 0
	s_nop 0
	s_nop 0
	s_nop 0
	s_nop 0
	s_nop 0
	s_nop 0
	s_barrier
	s_cbranch_scc1 .LBB0_2595
	v_mov_b32_e32 v109, v0
	v_readlane_b32 s0, v248, 56
	v_lshlrev_b32_e32 v2, 2, v109
	v_ashrrev_i32_e32 v3, 31, v2
	v_readlane_b32 s1, v248, 57
	s_barrier
	s_nop 0
	v_lshl_add_u64 v[2:3], v[2:3], 2, s[0:1]
	global_load_dwordx4 v[32:35], v[2:3], off
	v_add_co_u32_e32 v4, vcc, 0x2000, v2
	s_movk_i32 s0, 0x4000
	s_nop 0
	v_addc_co_u32_e32 v5, vcc, 0, v3, vcc
	global_load_dwordx4 v[26:29], v[4:5], off
	v_add_co_u32_e32 v4, vcc, s0, v2
	v_lshl_add_u32 v30, v109, 4, 0
	s_nop 0
	v_addc_co_u32_e32 v5, vcc, 0, v3, vcc
	global_load_dwordx4 v[22:25], v[4:5], off
	v_add_co_u32_e32 v4, vcc, 0x6000, v2
	v_readlane_b32 s0, v248, 49
	s_nop 0
	v_addc_co_u32_e32 v5, vcc, 0, v3, vcc
	global_load_dwordx4 v[18:21], v[4:5], off
	v_add_co_u32_e32 v4, vcc, 0x8000, v2
	v_readlane_b32 s1, v248, 50
	s_nop 0
	v_addc_co_u32_e32 v5, vcc, 0, v3, vcc
	global_load_dwordx4 v[14:17], v[4:5], off
	v_add_co_u32_e32 v4, vcc, 0xa000, v2
	v_readlane_b32 s2, v248, 58
	s_nop 0
	v_addc_co_u32_e32 v5, vcc, 0, v3, vcc
	global_load_dwordx4 v[10:13], v[4:5], off
	v_add_co_u32_e32 v4, vcc, 0xc000, v2
	v_readlane_b32 s3, v248, 59
	s_nop 0
	v_addc_co_u32_e32 v5, vcc, 0, v3, vcc
	global_load_dwordx4 v[6:9], v[4:5], off
	v_add_co_u32_e32 v2, vcc, 0xe000, v2
	s_waitcnt vmcnt(6)
	v_mul_f32_e32 v31, 0xbfb8aa3b, v32
	v_exp_f32_e32 v31, v31
	v_addc_co_u32_e32 v3, vcc, 0, v3, vcc
	global_load_dwordx4 v[2:5], v[2:3], off
	v_add_f32_e32 v31, 1.0, v31
	v_rcp_f32_e32 v36, v31
	v_mul_f32_e32 v31, 0xbfb8aa3b, v33
	v_exp_f32_e32 v31, v31
	s_andn2_b64 vcc, exec, s[0:1]
	v_add_f32_e32 v31, 1.0, v31
	v_rcp_f32_e32 v37, v31
	v_mul_f32_e32 v31, 0xbfb8aa3b, v34
	v_exp_f32_e32 v31, v31
	v_pk_mul_f32 v[32:33], v[32:33], v[36:37]
	v_add_f32_e32 v31, 1.0, v31
	v_rcp_f32_e32 v38, v31
	v_mul_f32_e32 v31, 0xbfb8aa3b, v35
	v_exp_f32_e32 v31, v31
	s_nop 0
	v_add_f32_e32 v31, 1.0, v31
	v_rcp_f32_e32 v39, v31
	s_waitcnt vmcnt(6)
	v_mul_f32_e32 v31, 0xbfb8aa3b, v26
	v_exp_f32_e32 v31, v31
	v_pk_mul_f32 v[34:35], v[34:35], v[38:39]
	ds_write_b128 v30, v[32:35]
	v_add_f32_e32 v31, 1.0, v31
	v_rcp_f32_e32 v32, v31
	v_mul_f32_e32 v31, 0xbfb8aa3b, v27
	v_exp_f32_e32 v31, v31
	s_nop 0
	v_add_f32_e32 v31, 1.0, v31
	v_rcp_f32_e32 v33, v31
	v_mul_f32_e32 v31, 0xbfb8aa3b, v28
	v_exp_f32_e32 v31, v31
	v_pk_mul_f32 v[26:27], v[26:27], v[32:33]
	v_add_f32_e32 v31, 1.0, v31
	v_rcp_f32_e32 v34, v31
	v_mul_f32_e32 v31, 0xbfb8aa3b, v29
	v_exp_f32_e32 v31, v31
	s_nop 0
	v_add_f32_e32 v31, 1.0, v31
	v_rcp_f32_e32 v35, v31
	s_nop 0
	v_pk_mul_f32 v[28:29], v[28:29], v[34:35]
	ds_write_b128 v30, v[26:29] offset:8192
	s_waitcnt vmcnt(5)
	v_mul_f32_e32 v26, 0xbfb8aa3b, v22
	v_mul_f32_e32 v27, 0xbfb8aa3b, v23
	v_mul_f32_e32 v28, 0xbfb8aa3b, v24
	v_mul_f32_e32 v29, 0xbfb8aa3b, v25
	v_exp_f32_e32 v26, v26
	v_exp_f32_e32 v27, v27
	v_exp_f32_e32 v28, v28
	v_exp_f32_e32 v29, v29
	v_add_f32_e32 v26, 1.0, v26
	v_add_f32_e32 v27, 1.0, v27
	v_add_f32_e32 v28, 1.0, v28
	v_add_f32_e32 v29, 1.0, v29
	v_rcp_f32_e32 v26, v26
	v_rcp_f32_e32 v27, v27
	v_rcp_f32_e32 v28, v28
	v_rcp_f32_e32 v29, v29
	v_pk_mul_f32 v[22:23], v[22:23], v[26:27]
	v_pk_mul_f32 v[24:25], v[24:25], v[28:29]
	ds_write_b128 v30, v[22:25] offset:16384
	s_waitcnt vmcnt(4)
	v_mul_f32_e32 v22, 0xbfb8aa3b, v18
	v_mul_f32_e32 v23, 0xbfb8aa3b, v19
	v_mul_f32_e32 v24, 0xbfb8aa3b, v20
	v_mul_f32_e32 v25, 0xbfb8aa3b, v21
	v_exp_f32_e32 v22, v22
	v_exp_f32_e32 v23, v23
	v_exp_f32_e32 v24, v24
	v_exp_f32_e32 v25, v25
	v_add_f32_e32 v22, 1.0, v22
	v_add_f32_e32 v23, 1.0, v23
	v_add_f32_e32 v24, 1.0, v24
	v_add_f32_e32 v25, 1.0, v25
	v_rcp_f32_e32 v22, v22
	v_rcp_f32_e32 v23, v23
	v_rcp_f32_e32 v24, v24
	v_rcp_f32_e32 v25, v25
	v_pk_mul_f32 v[18:19], v[18:19], v[22:23]
	v_pk_mul_f32 v[20:21], v[20:21], v[24:25]
	ds_write_b128 v30, v[18:21] offset:24576
	s_waitcnt vmcnt(3)
	v_mul_f32_e32 v18, 0xbfb8aa3b, v14
	v_mul_f32_e32 v19, 0xbfb8aa3b, v15
	v_mul_f32_e32 v20, 0xbfb8aa3b, v16
	v_mul_f32_e32 v21, 0xbfb8aa3b, v17
	v_exp_f32_e32 v18, v18
	v_exp_f32_e32 v19, v19
	v_exp_f32_e32 v20, v20
	v_exp_f32_e32 v21, v21
	v_add_f32_e32 v18, 1.0, v18
	v_add_f32_e32 v19, 1.0, v19
	v_add_f32_e32 v20, 1.0, v20
	v_add_f32_e32 v21, 1.0, v21
	v_rcp_f32_e32 v18, v18
	v_rcp_f32_e32 v19, v19
	v_rcp_f32_e32 v20, v20
	v_rcp_f32_e32 v21, v21
	v_pk_mul_f32 v[14:15], v[14:15], v[18:19]
	v_pk_mul_f32 v[16:17], v[16:17], v[20:21]
	ds_write_b128 v30, v[14:17] offset:32768
	s_waitcnt vmcnt(2)
	v_mul_f32_e32 v14, 0xbfb8aa3b, v10
	v_mul_f32_e32 v15, 0xbfb8aa3b, v11
	v_mul_f32_e32 v16, 0xbfb8aa3b, v12
	v_mul_f32_e32 v17, 0xbfb8aa3b, v13
	v_exp_f32_e32 v14, v14
	v_exp_f32_e32 v15, v15
	v_exp_f32_e32 v16, v16
	v_exp_f32_e32 v17, v17
	v_add_f32_e32 v14, 1.0, v14
	v_add_f32_e32 v15, 1.0, v15
	v_add_f32_e32 v16, 1.0, v16
	v_add_f32_e32 v17, 1.0, v17
	v_rcp_f32_e32 v14, v14
	v_rcp_f32_e32 v15, v15
	v_rcp_f32_e32 v16, v16
	v_rcp_f32_e32 v17, v17
	v_pk_mul_f32 v[10:11], v[10:11], v[14:15]
	v_pk_mul_f32 v[12:13], v[12:13], v[16:17]
	ds_write_b128 v30, v[10:13] offset:40960
	s_waitcnt vmcnt(1)
	v_mul_f32_e32 v10, 0xbfb8aa3b, v6
	v_mul_f32_e32 v11, 0xbfb8aa3b, v7
	v_mul_f32_e32 v12, 0xbfb8aa3b, v8
	v_mul_f32_e32 v13, 0xbfb8aa3b, v9
	v_exp_f32_e32 v10, v10
	v_exp_f32_e32 v11, v11
	v_exp_f32_e32 v12, v12
	v_exp_f32_e32 v13, v13
	v_add_f32_e32 v10, 1.0, v10
	v_add_f32_e32 v11, 1.0, v11
	v_add_f32_e32 v12, 1.0, v12
	v_add_f32_e32 v13, 1.0, v13
	v_rcp_f32_e32 v10, v10
	v_rcp_f32_e32 v11, v11
	v_rcp_f32_e32 v12, v12
	v_rcp_f32_e32 v13, v13
	v_pk_mul_f32 v[6:7], v[6:7], v[10:11]
	v_pk_mul_f32 v[8:9], v[8:9], v[12:13]
	ds_write_b128 v30, v[6:9] offset:49152
	s_waitcnt vmcnt(0)
	v_mul_f32_e32 v6, 0xbfb8aa3b, v2
	v_mul_f32_e32 v7, 0xbfb8aa3b, v3
	v_mul_f32_e32 v8, 0xbfb8aa3b, v4
	v_mul_f32_e32 v9, 0xbfb8aa3b, v5
	v_exp_f32_e32 v6, v6
	v_exp_f32_e32 v7, v7
	v_exp_f32_e32 v8, v8
	v_exp_f32_e32 v9, v9
	v_add_f32_e32 v6, 1.0, v6
	v_add_f32_e32 v7, 1.0, v7
	v_add_f32_e32 v8, 1.0, v8
	v_add_f32_e32 v9, 1.0, v9
	v_rcp_f32_e32 v6, v6
	v_rcp_f32_e32 v7, v7
	v_rcp_f32_e32 v8, v8
	v_rcp_f32_e32 v9, v9
	v_pk_mul_f32 v[2:3], v[2:3], v[6:7]
	v_pk_mul_f32 v[4:5], v[4:5], v[8:9]
	ds_write_b128 v30, v[2:5] offset:57344
	s_waitcnt lgkmcnt(0)
	s_barrier
	s_cbranch_vccnz .LBB0_2595
	s_movk_i32 s0, 0x1f8
	v_cmp_gt_i32_e32 vcc, s0, v109
	s_mov_b32 s0, 0x2aaaaaab
	v_mul_hi_i32 v111, v109, s0
	v_lshrrev_b32_e32 v113, 31, v111
	s_and_saveexec_b64 s[0:1], vcc
	s_cbranch_execz .LBB0_2592
	v_ashrrev_i32_e32 v2, 1, v111
	v_add_u32_e32 v115, v2, v113
	v_mul_lo_u32 v2, v115, 12
	v_sub_u32_e32 v2, v109, v2
	v_lshlrev_b32_e32 v2, 2, v2
	v_readlane_b32 s2, v248, 60
	v_ashrrev_i32_e32 v3, 31, v2
	v_readlane_b32 s3, v248, 61
	s_mov_b32 s4, 0xc000
	v_add_u32_e32 v117, 42, v115
	v_lshl_add_u64 v[62:63], v[2:3], 2, s[2:3]
	v_add_u32_e32 v119, 0x54, v115
	v_add_u32_e32 v121, 0x7e, v115
	v_add_u32_e32 v123, 0xa8, v115
	v_add_u32_e32 v125, 0xd2, v115
	v_add_u32_e32 v127, 0xfc, v115
	v_mad_i64_i32 v[2:3], s[2:3], v115, s4, v[62:63]
	v_mad_i64_i32 v[6:7], s[2:3], v117, s4, v[62:63]
	v_mad_i64_i32 v[10:11], s[2:3], v119, s4, v[62:63]
	v_mad_i64_i32 v[14:15], s[2:3], v121, s4, v[62:63]
	v_mad_i64_i32 v[18:19], s[2:3], v123, s4, v[62:63]
	v_mad_i64_i32 v[22:23], s[2:3], v125, s4, v[62:63]
	v_mad_i64_i32 v[26:27], s[2:3], v127, s4, v[62:63]
	global_load_dwordx4 v[2:5], v[2:3], off nt
	v_mov_b32_e32 v30, 0
	global_load_dwordx4 v[6:9], v[6:7], off nt
	s_mov_b32 s2, 0
	global_load_dwordx4 v[10:13], v[10:11], off nt
	v_mov_b32_e32 v31, v30
	global_load_dwordx4 v[14:17], v[14:15], off nt
	v_mov_b32_e32 v32, v30
	global_load_dwordx4 v[18:21], v[18:19], off nt
	v_mov_b32_e32 v33, v30
	global_load_dwordx4 v[22:25], v[22:23], off nt
	v_mov_b32_e32 v54, v30
	global_load_dwordx4 v[26:29], v[26:27], off nt
	v_mov_b32_e32 v55, v30
	v_mov_b32_e32 v56, v30
	v_mov_b32_e32 v57, v30
	v_mov_b32_e32 v50, v30
	v_mov_b32_e32 v51, v30
	v_mov_b32_e32 v52, v30
	v_mov_b32_e32 v53, v30
	v_mov_b32_e32 v46, v30
	v_mov_b32_e32 v47, v30
	v_mov_b32_e32 v48, v30
	v_mov_b32_e32 v49, v30
	v_mov_b32_e32 v42, v30
	v_mov_b32_e32 v43, v30
	v_mov_b32_e32 v44, v30
	v_mov_b32_e32 v45, v30
	v_mov_b32_e32 v38, v30
	v_mov_b32_e32 v39, v30
	v_mov_b32_e32 v40, v30
	v_mov_b32_e32 v41, v30
	v_mov_b32_e32 v34, v30
	v_mov_b32_e32 v35, v30
	v_mov_b32_e32 v36, v30
	v_mov_b32_e32 v37, v30
	v_mov_b32_e32 v58, v30
	v_mov_b32_e32 v59, v30
	v_mov_b32_e32 v60, v30
	v_mov_b32_e32 v61, v30
	s_waitcnt vmcnt(6)
	v_mov_b32_e32 v64, v2
	v_mov_b32_e32 v65, v3
	v_mov_b32_e32 v82, v4
	v_mov_b32_e32 v83, v5
	s_waitcnt vmcnt(5)
	v_mov_b32_e32 v84, v6
	v_mov_b32_e32 v85, v7
	v_mov_b32_e32 v86, v8
	v_mov_b32_e32 v87, v9
	s_waitcnt vmcnt(4)
	v_mov_b32_e32 v88, v10
	v_mov_b32_e32 v89, v11
	v_mov_b32_e32 v90, v12
	v_mov_b32_e32 v91, v13
	s_waitcnt vmcnt(3)
	v_mov_b32_e32 v92, v14
	v_mov_b32_e32 v93, v15
	v_mov_b32_e32 v94, v16
	v_mov_b32_e32 v95, v17
	s_waitcnt vmcnt(2)
	v_mov_b32_e32 v96, v18
	v_mov_b32_e32 v97, v19
	v_mov_b32_e32 v98, v20
	v_mov_b32_e32 v99, v21
	s_waitcnt vmcnt(1)
	v_mov_b32_e32 v100, v22
	v_mov_b32_e32 v101, v23
	v_mov_b32_e32 v102, v24
	v_mov_b32_e32 v103, v25
	s_waitcnt vmcnt(0)
	v_mov_b32_e32 v104, v26
	v_mov_b32_e32 v105, v27
	v_mov_b32_e32 v106, v28
	v_mov_b32_e32 v107, v29
	s_branch .LBB0_2477
